# v082 + MoBA QK^T MFMAs accumulator-stationary (8 on p0 then 8 on p1) in the two hot MoBA loops
# baseline (speedup 1.0000x reference)
.LBB0_215:
	s_mov_b32 m0, s81
	s_add_i32 s5, s89, 0xfeffff80
	buffer_load_dwordx4 v186, s[92:95], s5 offen lds
	s_add_i32 s5, s89, 0xff001f80
	s_mov_b32 m0, s66
	s_add_i32 s6, s89, 0xffffff80
	buffer_load_dwordx4 v186, s[92:95], s5 offen lds
	s_add_i32 s5, s75, s77
	s_mov_b32 m0, s5
	s_nop 0
	buffer_load_dwordx4 v197, s[92:95], s6 offen lds
	s_add_i32 m0, s5, 0x400
	s_nop 0
	buffer_load_dwordx4 v197, s[92:95], s89 offen lds
	v_exp_f32_e32 v116, v98
	v_exp_f32_e32 v120, v1
	v_exp_f32_e32 v118, v106
	v_exp_f32_e32 v124, v107
	v_exp_f32_e32 v122, v100
	v_exp_f32_e32 v126, v108
	v_exp_f32_e32 v128, v101
	v_exp_f32_e32 v164, v109
	v_exp_f32_e32 v162, v102
	v_exp_f32_e32 v166, v110
	v_exp_f32_e32 v168, v103
	v_exp_f32_e32 v172, v111
	v_add_f32_e32 v1, v117, v125
	v_add_f32_e32 v66, v115, v123
	v_add_f32_e32 v67, v116, v120
	v_add_f32_e32 v68, v118, v124
	v_exp_f32_e32 v170, v104
	v_exp_f32_e32 v174, v112
	v_add_f32_e32 v1, v121, v1
	v_add_f32_e32 v66, v119, v66
	v_add_f32_e32 v67, v122, v67
	v_add_f32_e32 v68, v126, v68
	v_exp_f32_e32 v176, v105
	v_exp_f32_e32 v213, v113
	v_add_f32_e32 v1, v165, v1
	v_add_f32_e32 v66, v163, v66
	v_add_f32_e32 v67, v128, v67
	v_add_f32_e32 v68, v164, v68
	v_add_f32_e32 v1, v129, v1
	v_add_f32_e32 v66, v127, v66
	v_add_f32_e32 v67, v162, v67
	v_add_f32_e32 v68, v166, v68
	v_add_f32_e32 v1, v173, v1
	v_add_f32_e32 v66, v171, v66
	v_add_f32_e32 v67, v168, v67
	v_add_f32_e32 v68, v172, v68
	v_add_f32_e32 v1, v169, v1
	v_add_f32_e32 v66, v167, v66
	v_add_f32_e32 v67, v170, v67
	v_add_f32_e32 v68, v174, v68
	v_add_f32_e32 v1, v177, v1
	v_add_f32_e32 v66, v175, v66
	v_add_f32_e32 v67, v176, v67
	v_add_f32_e32 v68, v213, v68
	v_add_f32_e32 v1, v66, v1
	v_add_f32_e32 v66, v68, v67
	v_add_f32_e32 v1, v1, v66
	v_mov_b32_e32 v212, v1
	s_nop 1
	v_permlane32_swap_b32_e32 v1, v212
	ds_read_b128 v[86:89], v207 offset:256
	ds_read_b128 v[90:93], v207 offset:288
	ds_read_b128 v[70:73], v207 offset:384
	ds_read_b128 v[74:77], v207 offset:416
	ds_read_b128 v[94:97], v207 offset:320
	ds_read_b128 v[98:101], v207 offset:352
	ds_read_b128 v[78:81], v207 offset:448
	ds_read_b128 v[82:85], v207 offset:480
	ds_read_b128 v[66:69], v208
	ds_read_b128 v[102:105], v209
	ds_read_b128 v[106:109], v210
	ds_read_b128 v[110:113], v211
	ds_read_b128 v[214:217], v208 offset:128
	ds_read_b128 v[218:221], v209 offset:128
	ds_read_b128 v[222:225], v210 offset:128
	ds_read_b128 v[226:229], v211 offset:128
	s_waitcnt lgkmcnt(7)
	v_mfma_f32_32x32x16_bf16 v[86:101], v[66:69], v[158:161], v[86:101]
	ds_read_b128 v[66:69], v208 offset:8192
	ds_read_b128 v[230:233], v209 offset:8192
	s_waitcnt lgkmcnt(8)
	v_mfma_f32_32x32x16_bf16 v[86:101], v[102:105], v[154:157], v[86:101]
	ds_read_b128 v[102:105], v210 offset:8192
	s_waitcnt lgkmcnt(8)
	v_mfma_f32_32x32x16_bf16 v[86:101], v[106:109], v[150:153], v[86:101]
	ds_read_b128 v[106:109], v211 offset:8192
	s_waitcnt lgkmcnt(8)
	v_mfma_f32_32x32x16_bf16 v[86:101], v[110:113], v[146:149], v[86:101]
	ds_read_b128 v[110:113], v208 offset:8320
	s_waitcnt lgkmcnt(8)
	v_mfma_f32_32x32x16_bf16 v[86:101], v[214:217], v[142:145], v[86:101]
	ds_read_b128 v[214:217], v209 offset:8320
	s_waitcnt lgkmcnt(8)
	v_mfma_f32_32x32x16_bf16 v[86:101], v[218:221], v[138:141], v[86:101]
	ds_read_b128 v[218:221], v210 offset:8320
	s_waitcnt lgkmcnt(8)
	v_mfma_f32_32x32x16_bf16 v[86:101], v[222:225], v[134:137], v[86:101]
	ds_read_b128 v[222:225], v211 offset:8320
	s_waitcnt lgkmcnt(8)
	v_mfma_f32_32x32x16_bf16 v[86:101], v[226:229], v[130:133], v[86:101]
	s_waitcnt lgkmcnt(7)
	v_mfma_f32_32x32x16_bf16 v[70:85], v[66:69], v[158:161], v[70:85]
	s_waitcnt lgkmcnt(6)
	v_mfma_f32_32x32x16_bf16 v[70:85], v[230:233], v[154:157], v[70:85]
	s_waitcnt lgkmcnt(5)
	v_mfma_f32_32x32x16_bf16 v[70:85], v[102:105], v[150:153], v[70:85]
	s_waitcnt lgkmcnt(4)
	v_mfma_f32_32x32x16_bf16 v[70:85], v[106:109], v[146:149], v[70:85]
	s_waitcnt lgkmcnt(3)
	v_mfma_f32_32x32x16_bf16 v[70:85], v[110:113], v[142:145], v[70:85]
	s_waitcnt lgkmcnt(2)
	v_mfma_f32_32x32x16_bf16 v[70:85], v[214:217], v[138:141], v[70:85]
	s_waitcnt lgkmcnt(1)
	v_mfma_f32_32x32x16_bf16 v[70:85], v[218:221], v[134:137], v[70:85]
	s_waitcnt lgkmcnt(0)
	v_mfma_f32_32x32x16_bf16 v[70:85], v[222:225], v[130:133], v[70:85]
	v_add_u32_e32 v114, s4, v190
	ds_read_b64_tr_b16 v[110:111], v114 offset:0
	ds_read_b64_tr_b16 v[112:113], v114 offset:0x800
	ds_read_b64_tr_b16 v[106:107], v114 offset:0x1000
	ds_read_b64_tr_b16 v[108:109], v114 offset:0x1800
	ds_read_b64_tr_b16 v[102:103], v114 offset:0x2000
	ds_read_b64_tr_b16 v[104:105], v114 offset:0x2800
	ds_read_b64_tr_b16 v[66:67], v114 offset:0x3000
	ds_read_b64_tr_b16 v[68:69], v114 offset:0x3800
	s_add_i32 s4, s88, 64
	s_cmp_le_i32 s4, s70
	s_cbranch_scc1 .LBB0_217
	v_subrev_u32_e32 v214, 64, v206
	v_cmp_gt_i32_e64 s[62:63], 26, v214
	v_cmp_gt_i32_e64 s[64:65], 27, v214
	v_cmp_gt_i32_e64 s[60:61], 25, v214
	s_and_b64 s[62:63], s[64:65], s[62:63]
	v_cmp_gt_i32_e64 s[58:59], 24, v214
	s_and_b64 s[60:61], s[62:63], s[60:61]
	v_cmp_gt_i32_e64 s[56:57], 19, v214
	s_and_b64 s[58:59], s[60:61], s[58:59]
	v_cmp_gt_i32_e64 s[54:55], 18, v214
	s_and_b64 s[56:57], s[58:59], s[56:57]
	v_cmp_gt_i32_e64 s[52:53], 17, v214
	s_and_b64 s[54:55], s[56:57], s[54:55]
	v_cmp_gt_i32_e64 s[50:51], 16, v214
	s_and_b64 s[52:53], s[54:55], s[52:53]
	v_cmp_gt_i32_e64 s[48:49], 11, v214
	s_and_b64 s[50:51], s[52:53], s[50:51]
	v_cmp_gt_i32_e64 s[46:47], 10, v214
	s_and_b64 s[48:49], s[50:51], s[48:49]
	v_cmp_gt_i32_e64 s[44:45], 9, v214
	s_and_b64 s[46:47], s[48:49], s[46:47]
	v_cmp_gt_i32_e64 s[42:43], 8, v214
	s_and_b64 s[44:45], s[46:47], s[44:45]
	v_cmp_gt_i32_e64 s[40:41], 3, v214
	s_and_b64 s[42:43], s[44:45], s[42:43]
	v_cmp_gt_i32_e64 s[38:39], 2, v214
	s_and_b64 s[40:41], s[42:43], s[40:41]
	v_cmp_gt_i32_e64 s[36:37], 1, v214
	s_and_b64 s[38:39], s[40:41], s[38:39]
	v_cmp_gt_i32_e64 s[34:35], 0, v214
	s_and_b64 s[36:37], s[38:39], s[36:37]
	s_and_b64 s[34:35], s[36:37], s[34:35]
	v_cmp_gt_i32_e64 s[30:31], 58, v214
	v_cndmask_b32_e64 v86, v86, v183, s[34:35]
	v_cmp_gt_i32_e64 s[34:35], 59, v214
	v_cmp_gt_i32_e64 s[28:29], 57, v214
	s_and_b64 s[30:31], s[34:35], s[30:31]
	v_cmp_gt_i32_e64 s[26:27], 56, v214
	s_and_b64 s[28:29], s[30:31], s[28:29]
	v_cmp_gt_i32_e64 s[24:25], 51, v214
	s_and_b64 s[26:27], s[28:29], s[26:27]
	v_cmp_gt_i32_e64 s[22:23], 50, v214
	s_and_b64 s[24:25], s[26:27], s[24:25]
	v_cmp_gt_i32_e64 s[20:21], 49, v214
	s_and_b64 s[22:23], s[24:25], s[22:23]
	v_cmp_gt_i32_e64 s[18:19], 48, v214
	s_and_b64 s[20:21], s[22:23], s[20:21]
	v_cmp_gt_i32_e64 s[16:17], 43, v214
	s_and_b64 s[18:19], s[20:21], s[18:19]
	v_cmp_gt_i32_e64 s[14:15], 42, v214
	s_and_b64 s[16:17], s[18:19], s[16:17]
	v_cmp_gt_i32_e64 s[12:13], 41, v214
	s_and_b64 s[14:15], s[16:17], s[14:15]
	v_cmp_gt_i32_e64 s[10:11], 40, v214
	s_and_b64 s[12:13], s[14:15], s[12:13]
	v_cmp_gt_i32_e64 s[8:9], 35, v214
	s_and_b64 s[10:11], s[12:13], s[10:11]
	v_cmp_gt_i32_e64 s[6:7], 34, v214
	s_and_b64 s[8:9], s[10:11], s[8:9]
	v_cmp_gt_i32_e64 s[4:5], 33, v214
	s_and_b64 s[6:7], s[8:9], s[6:7]
	v_cmp_gt_i32_e32 vcc, 32, v214
	s_and_b64 s[4:5], s[6:7], s[4:5]
	s_and_b64 vcc, s[4:5], vcc
	v_cndmask_b32_e64 v101, v101, v183, s[64:65]
	v_cndmask_b32_e64 v100, v100, v183, s[62:63]
	v_cndmask_b32_e64 v99, v99, v183, s[60:61]
	v_cndmask_b32_e64 v98, v98, v183, s[58:59]
	v_cndmask_b32_e64 v97, v97, v183, s[56:57]
	v_cndmask_b32_e64 v96, v96, v183, s[54:55]
	v_cndmask_b32_e64 v95, v95, v183, s[52:53]
	v_cndmask_b32_e64 v94, v94, v183, s[50:51]
	v_cndmask_b32_e64 v93, v93, v183, s[48:49]
	v_cndmask_b32_e64 v92, v92, v183, s[46:47]
	v_cndmask_b32_e64 v91, v91, v183, s[44:45]
	v_cndmask_b32_e64 v90, v90, v183, s[42:43]
	v_cndmask_b32_e64 v89, v89, v183, s[40:41]
	v_cndmask_b32_e64 v88, v88, v183, s[38:39]
	v_cndmask_b32_e64 v87, v87, v183, s[36:37]
	v_cndmask_b32_e64 v85, v85, v183, s[34:35]
	v_cndmask_b32_e64 v84, v84, v183, s[30:31]
	v_cndmask_b32_e64 v83, v83, v183, s[28:29]
	v_cndmask_b32_e64 v82, v82, v183, s[26:27]
	v_cndmask_b32_e64 v81, v81, v183, s[24:25]
	v_cndmask_b32_e64 v80, v80, v183, s[22:23]
	v_cndmask_b32_e64 v79, v79, v183, s[20:21]
	v_cndmask_b32_e64 v78, v78, v183, s[18:19]
	v_cndmask_b32_e64 v77, v77, v183, s[16:17]
	v_cndmask_b32_e64 v76, v76, v183, s[14:15]
	v_cndmask_b32_e64 v75, v75, v183, s[12:13]
	v_cndmask_b32_e64 v74, v74, v183, s[10:11]
	v_cndmask_b32_e64 v73, v73, v183, s[8:9]
	v_cndmask_b32_e64 v72, v72, v183, s[6:7]
	v_cndmask_b32_e64 v71, v71, v183, s[4:5]
	v_cndmask_b32_e32 v70, v70, v183, vcc

.LBB0_223:
	v_cndmask_b32_e64 v216, v115, v196, s[4:5]
	v_sub_f32_e32 v66, v86, v216
	v_sub_f32_e32 v67, v87, v216
	v_sub_f32_e32 v68, v88, v216
	v_sub_f32_e32 v69, v89, v216
	v_sub_f32_e32 v86, v90, v216
	v_sub_f32_e32 v87, v91, v216
	v_sub_f32_e32 v88, v92, v216
	v_sub_f32_e32 v89, v93, v216
	v_sub_f32_e32 v90, v94, v216
	v_sub_f32_e32 v91, v95, v216
	v_sub_f32_e32 v92, v96, v216
	v_sub_f32_e32 v93, v97, v216
	v_sub_f32_e32 v94, v98, v216
	v_sub_f32_e32 v95, v99, v216
	v_sub_f32_e32 v96, v100, v216
	v_sub_f32_e32 v97, v101, v216
	v_sub_f32_e32 v98, v70, v216
	v_sub_f32_e32 v99, v71, v216
	v_sub_f32_e32 v100, v72, v216
	v_sub_f32_e32 v101, v73, v216
	v_sub_f32_e32 v102, v74, v216
	v_sub_f32_e32 v103, v75, v216
	v_sub_f32_e32 v104, v76, v216
	v_sub_f32_e32 v105, v77, v216
	v_sub_f32_e32 v106, v78, v216
	v_sub_f32_e32 v107, v79, v216
	v_sub_f32_e32 v108, v80, v216
	v_sub_f32_e32 v109, v81, v216
	v_exp_f32_e32 v66, v66
	v_exp_f32_e32 v67, v67
	v_exp_f32_e32 v68, v68
	v_exp_f32_e32 v69, v69
	v_exp_f32_e32 v70, v86
	v_exp_f32_e32 v71, v87
	v_exp_f32_e32 v72, v88
	v_exp_f32_e32 v73, v89
	v_exp_f32_e32 v74, v90
	v_exp_f32_e32 v75, v91
	v_exp_f32_e32 v76, v92
	v_exp_f32_e32 v77, v93
	v_exp_f32_e32 v78, v94
	v_exp_f32_e32 v79, v95
	v_exp_f32_e32 v80, v96
	v_exp_f32_e32 v81, v97
	v_sub_f32_e32 v110, v82, v216
	v_sub_f32_e32 v95, v83, v216
	v_sub_f32_e32 v96, v84, v216
	v_sub_f32_e32 v97, v85, v216
	v_exp_f32_e32 v82, v98
	v_exp_f32_e32 v83, v99
	v_exp_f32_e32 v90, v106
	v_exp_f32_e32 v91, v107
	v_exp_f32_e32 v84, v100
	v_exp_f32_e32 v92, v108
	v_exp_f32_e32 v85, v101
	v_exp_f32_e32 v93, v109
	v_exp_f32_e32 v86, v102
	v_exp_f32_e32 v94, v110
	v_exp_f32_e32 v87, v103
	v_exp_f32_e32 v95, v95
	v_add_f32_e32 v98, v66, v67
	v_add_f32_e32 v99, v74, v75
	v_add_f32_e32 v100, v82, v83
	v_add_f32_e32 v101, v90, v91
	v_exp_f32_e32 v88, v104
	v_exp_f32_e32 v96, v96
	v_add_f32_e32 v98, v68, v98
	v_add_f32_e32 v99, v76, v99
	v_add_f32_e32 v100, v84, v100
	v_add_f32_e32 v101, v92, v101
	v_exp_f32_e32 v89, v105
	v_exp_f32_e32 v97, v97
	v_add_f32_e32 v98, v69, v98
	v_add_f32_e32 v99, v77, v99
	v_add_f32_e32 v100, v85, v100
	v_add_f32_e32 v101, v93, v101
	v_add_f32_e32 v98, v70, v98
	v_add_f32_e32 v99, v78, v99
	v_add_f32_e32 v100, v86, v100
	v_add_f32_e32 v101, v94, v101
	v_add_f32_e32 v98, v71, v98
	v_add_f32_e32 v99, v79, v99
	v_add_f32_e32 v100, v87, v100
	v_add_f32_e32 v101, v95, v101
	v_add_f32_e32 v98, v72, v98
	v_add_f32_e32 v99, v80, v99
	v_add_f32_e32 v100, v88, v100
	v_add_f32_e32 v101, v96, v101
	v_add_f32_e32 v98, v73, v98
	v_add_f32_e32 v99, v81, v99
	v_add_f32_e32 v100, v89, v100
	v_add_f32_e32 v101, v97, v101
	v_add_f32_e32 v98, v99, v98
	v_add_f32_e32 v99, v101, v100
	v_add_f32_e32 v214, v99, v98
	v_mov_b32_e32 v215, v214
	s_nop 1
	v_permlane32_swap_b32_e32 v214, v215
	ds_read_b128 v[114:117], v207
	ds_read_b128 v[118:121], v207 offset:32
	ds_read_b128 v[98:101], v207 offset:128
	ds_read_b128 v[102:105], v207 offset:160
	ds_read_b128 v[122:125], v207 offset:64
	ds_read_b128 v[126:129], v207 offset:96
	ds_read_b128 v[106:109], v207 offset:192
	ds_read_b128 v[110:113], v207 offset:224
	ds_read_b128 v[162:165], v199 offset:49152
	ds_read_b128 v[166:169], v200 offset:49152
	ds_read_b128 v[170:173], v201 offset:49152
	ds_read_b128 v[174:177], v202 offset:49152
	ds_read_b128 v[218:221], v199 offset:49280
	ds_read_b128 v[222:225], v200 offset:49280
	ds_read_b128 v[226:229], v201 offset:49280
	ds_read_b128 v[230:233], v202 offset:49280
	s_waitcnt lgkmcnt(7)
	v_mfma_f32_32x32x16_bf16 v[114:129], v[162:165], v[158:161], v[114:129]
	ds_read_b128 v[162:165], v199 offset:57344
	ds_read_b128 v[234:237], v200 offset:57344
	s_waitcnt lgkmcnt(8)
	v_mfma_f32_32x32x16_bf16 v[114:129], v[166:169], v[154:157], v[114:129]
	ds_read_b128 v[166:169], v201 offset:57344
	s_waitcnt lgkmcnt(8)
	v_mfma_f32_32x32x16_bf16 v[114:129], v[170:173], v[150:153], v[114:129]
	ds_read_b128 v[170:173], v202 offset:57344
	s_waitcnt lgkmcnt(8)
	v_mfma_f32_32x32x16_bf16 v[114:129], v[174:177], v[146:149], v[114:129]
	ds_read_b128 v[174:177], v199 offset:57472
	s_waitcnt lgkmcnt(8)
	v_mfma_f32_32x32x16_bf16 v[114:129], v[218:221], v[142:145], v[114:129]
	ds_read_b128 v[218:221], v200 offset:57472
	s_waitcnt lgkmcnt(8)
	v_mfma_f32_32x32x16_bf16 v[114:129], v[222:225], v[138:141], v[114:129]
	ds_read_b128 v[222:225], v201 offset:57472
	s_waitcnt lgkmcnt(8)
	v_mfma_f32_32x32x16_bf16 v[114:129], v[226:229], v[134:137], v[114:129]
	ds_read_b128 v[226:229], v202 offset:57472
	s_waitcnt lgkmcnt(8)
	v_mfma_f32_32x32x16_bf16 v[114:129], v[230:233], v[130:133], v[114:129]
	s_waitcnt lgkmcnt(7)
	v_mfma_f32_32x32x16_bf16 v[98:113], v[162:165], v[158:161], v[98:113]
	s_waitcnt lgkmcnt(6)
	v_mfma_f32_32x32x16_bf16 v[98:113], v[234:237], v[154:157], v[98:113]
	s_waitcnt lgkmcnt(5)
	v_mfma_f32_32x32x16_bf16 v[98:113], v[166:169], v[150:153], v[98:113]
	s_waitcnt lgkmcnt(4)
	v_mfma_f32_32x32x16_bf16 v[98:113], v[170:173], v[146:149], v[98:113]
	s_waitcnt lgkmcnt(3)
	v_mfma_f32_32x32x16_bf16 v[98:113], v[174:177], v[142:145], v[98:113]
	s_waitcnt lgkmcnt(2)
	v_mfma_f32_32x32x16_bf16 v[98:113], v[218:221], v[138:141], v[98:113]
	s_waitcnt lgkmcnt(1)
	v_mfma_f32_32x32x16_bf16 v[98:113], v[222:225], v[134:137], v[98:113]
	s_waitcnt lgkmcnt(0)
	v_mfma_f32_32x32x16_bf16 v[98:113], v[226:229], v[130:133], v[98:113]
	v_add_u32_e32 v196, s33, v190
	ds_read_b64_tr_b16 v[174:175], v196 offset:0
	ds_read_b64_tr_b16 v[176:177], v196 offset:0x800
	ds_read_b64_tr_b16 v[170:171], v196 offset:0x1000
	ds_read_b64_tr_b16 v[172:173], v196 offset:0x1800
	ds_read_b64_tr_b16 v[166:167], v196 offset:0x2000
	ds_read_b64_tr_b16 v[168:169], v196 offset:0x2800
	ds_read_b64_tr_b16 v[162:163], v196 offset:0x3000
	ds_read_b64_tr_b16 v[164:165], v196 offset:0x3800
	s_cmp_le_i32 s88, s70
	s_cbranch_scc1 .LBB0_225
	v_cmp_gt_i32_e64 s[62:63], 26, v206
	v_cmp_gt_i32_e64 s[64:65], 27, v206
	v_cmp_gt_i32_e64 s[60:61], 25, v206
	s_and_b64 s[62:63], s[64:65], s[62:63]
	v_cmp_gt_i32_e64 s[58:59], 24, v206
	s_and_b64 s[60:61], s[62:63], s[60:61]
	v_cmp_gt_i32_e64 s[56:57], 19, v206
	s_and_b64 s[58:59], s[60:61], s[58:59]
	v_cmp_gt_i32_e64 s[54:55], 18, v206
	s_and_b64 s[56:57], s[58:59], s[56:57]
	v_cmp_gt_i32_e64 s[52:53], 17, v206
	s_and_b64 s[54:55], s[56:57], s[54:55]
	v_cmp_gt_i32_e64 s[50:51], 16, v206
	s_and_b64 s[52:53], s[54:55], s[52:53]
	v_cmp_gt_i32_e64 s[48:49], 11, v206
	s_and_b64 s[50:51], s[52:53], s[50:51]
	v_cmp_gt_i32_e64 s[46:47], 10, v206
	s_and_b64 s[48:49], s[50:51], s[48:49]
	v_cmp_gt_i32_e64 s[44:45], 9, v206
	s_and_b64 s[46:47], s[48:49], s[46:47]
	v_cmp_gt_i32_e64 s[42:43], 8, v206
	s_and_b64 s[44:45], s[46:47], s[44:45]
	v_cmp_gt_i32_e64 s[40:41], 3, v206
	s_and_b64 s[42:43], s[44:45], s[42:43]
	v_cmp_gt_i32_e64 s[38:39], 2, v206
	s_and_b64 s[40:41], s[42:43], s[40:41]
	v_cmp_gt_i32_e64 s[36:37], 1, v206
	s_and_b64 s[38:39], s[40:41], s[38:39]
	v_cmp_gt_i32_e64 s[34:35], 0, v206
	s_and_b64 s[36:37], s[38:39], s[36:37]
	s_and_b64 s[34:35], s[36:37], s[34:35]
	v_cmp_gt_i32_e64 s[30:31], 58, v206
	v_cndmask_b32_e64 v114, v114, v183, s[34:35]
	v_cmp_gt_i32_e64 s[34:35], 59, v206
	v_cmp_gt_i32_e64 s[28:29], 57, v206
	s_and_b64 s[30:31], s[34:35], s[30:31]
	v_cmp_gt_i32_e64 s[26:27], 56, v206
	s_and_b64 s[28:29], s[30:31], s[28:29]
	v_cmp_gt_i32_e64 s[24:25], 51, v206
	s_and_b64 s[26:27], s[28:29], s[26:27]
	v_cmp_gt_i32_e64 s[22:23], 50, v206
	s_and_b64 s[24:25], s[26:27], s[24:25]
	v_cmp_gt_i32_e64 s[20:21], 49, v206
	s_and_b64 s[22:23], s[24:25], s[22:23]
	v_cmp_gt_i32_e64 s[18:19], 48, v206
	s_and_b64 s[20:21], s[22:23], s[20:21]
	v_cmp_gt_i32_e64 s[16:17], 43, v206
	s_and_b64 s[18:19], s[20:21], s[18:19]
	v_cmp_gt_i32_e64 s[14:15], 42, v206
	s_and_b64 s[16:17], s[18:19], s[16:17]
	v_cmp_gt_i32_e64 s[12:13], 41, v206
	s_and_b64 s[14:15], s[16:17], s[14:15]
	v_cmp_gt_i32_e64 s[10:11], 40, v206
	s_and_b64 s[12:13], s[14:15], s[12:13]
	v_cmp_gt_i32_e64 s[8:9], 35, v206
	s_and_b64 s[10:11], s[12:13], s[10:11]
	v_cmp_gt_i32_e64 s[6:7], 34, v206
	s_and_b64 s[8:9], s[10:11], s[8:9]
	v_cmp_gt_i32_e64 s[4:5], 33, v206
	s_and_b64 s[6:7], s[8:9], s[6:7]
	v_cmp_gt_i32_e32 vcc, 32, v206
	s_and_b64 s[4:5], s[6:7], s[4:5]
	s_and_b64 vcc, s[4:5], vcc
	v_cndmask_b32_e64 v129, v129, v183, s[64:65]
	v_cndmask_b32_e64 v128, v128, v183, s[62:63]
	v_cndmask_b32_e64 v127, v127, v183, s[60:61]
	v_cndmask_b32_e64 v126, v126, v183, s[58:59]
	v_cndmask_b32_e64 v125, v125, v183, s[56:57]
	v_cndmask_b32_e64 v124, v124, v183, s[54:55]
	v_cndmask_b32_e64 v123, v123, v183, s[52:53]
	v_cndmask_b32_e64 v122, v122, v183, s[50:51]
	v_cndmask_b32_e64 v121, v121, v183, s[48:49]
	v_cndmask_b32_e64 v120, v120, v183, s[46:47]
	v_cndmask_b32_e64 v119, v119, v183, s[44:45]
	v_cndmask_b32_e64 v118, v118, v183, s[42:43]
	v_cndmask_b32_e64 v117, v117, v183, s[40:41]
	v_cndmask_b32_e64 v116, v116, v183, s[38:39]
	v_cndmask_b32_e64 v115, v115, v183, s[36:37]
	v_cndmask_b32_e64 v113, v113, v183, s[34:35]
	v_cndmask_b32_e64 v112, v112, v183, s[30:31]
	v_cndmask_b32_e64 v111, v111, v183, s[28:29]
	v_cndmask_b32_e64 v110, v110, v183, s[26:27]
	v_cndmask_b32_e64 v109, v109, v183, s[24:25]
	v_cndmask_b32_e64 v108, v108, v183, s[22:23]
	v_cndmask_b32_e64 v107, v107, v183, s[20:21]
	v_cndmask_b32_e64 v106, v106, v183, s[18:19]
	v_cndmask_b32_e64 v105, v105, v183, s[16:17]
	v_cndmask_b32_e64 v104, v104, v183, s[14:15]
	v_cndmask_b32_e64 v103, v103, v183, s[12:13]
	v_cndmask_b32_e64 v102, v102, v183, s[10:11]
	v_cndmask_b32_e64 v101, v101, v183, s[8:9]
	v_cndmask_b32_e64 v100, v100, v183, s[6:7]
	v_cndmask_b32_e64 v99, v99, v183, s[4:5]
	v_cndmask_b32_e32 v98, v98, v183, vcc

.LBB0_260:
	s_mov_b32 m0, s84
	s_add_i32 s5, s97, 0xfeffff80
	buffer_load_dwordx4 v202, s[92:95], s5 offen lds
	s_add_i32 s5, s97, 0xff001f80
	s_mov_b32 m0, s85
	s_add_i32 s6, s97, 0xffffff80
	buffer_load_dwordx4 v202, s[92:95], s5 offen lds
	s_add_i32 s5, s82, s69
	s_mov_b32 m0, s5
	s_nop 0
	buffer_load_dwordx4 v186, s[92:95], s6 offen lds
	s_add_i32 m0, s5, 0x400
	s_nop 0
	buffer_load_dwordx4 v186, s[92:95], s97 offen lds
	ds_read_b128 v[114:117], v213 offset:256
	ds_read_b128 v[118:121], v213 offset:288
	ds_read_b128 v[70:73], v213 offset:384
	ds_read_b128 v[74:77], v213 offset:416
	ds_read_b128 v[122:125], v213 offset:320
	ds_read_b128 v[126:129], v213 offset:352
	ds_read_b128 v[78:81], v213 offset:448
	ds_read_b128 v[82:85], v213 offset:480
	ds_read_b128 v[66:69], v214
	ds_read_b128 v[86:89], v215
	ds_read_b128 v[90:93], v216
	ds_read_b128 v[94:97], v217
	ds_read_b128 v[218:221], v214 offset:128
	ds_read_b128 v[222:225], v215 offset:128
	ds_read_b128 v[226:229], v216 offset:128
	ds_read_b128 v[230:233], v217 offset:128
	s_waitcnt lgkmcnt(7)
	v_mfma_f32_32x32x16_bf16 v[114:129], v[66:69], v[170:173], v[114:129]
	ds_read_b128 v[66:69], v214 offset:8192
	ds_read_b128 v[234:237], v215 offset:8192
	s_waitcnt lgkmcnt(8)
	v_mfma_f32_32x32x16_bf16 v[114:129], v[86:89], v[166:169], v[114:129]
	ds_read_b128 v[86:89], v216 offset:8192
	s_waitcnt lgkmcnt(8)
	v_mfma_f32_32x32x16_bf16 v[114:129], v[90:93], v[162:165], v[114:129]
	ds_read_b128 v[90:93], v217 offset:8192
	s_waitcnt lgkmcnt(8)
	v_mfma_f32_32x32x16_bf16 v[114:129], v[94:97], v[158:161], v[114:129]
	ds_read_b128 v[94:97], v214 offset:8320
	s_waitcnt lgkmcnt(8)
	v_mfma_f32_32x32x16_bf16 v[114:129], v[218:221], v[154:157], v[114:129]
	ds_read_b128 v[218:221], v215 offset:8320
	s_waitcnt lgkmcnt(8)
	v_mfma_f32_32x32x16_bf16 v[114:129], v[222:225], v[150:153], v[114:129]
	ds_read_b128 v[222:225], v216 offset:8320
	s_waitcnt lgkmcnt(8)
	v_mfma_f32_32x32x16_bf16 v[114:129], v[226:229], v[146:149], v[114:129]
	ds_read_b128 v[226:229], v217 offset:8320
	s_waitcnt lgkmcnt(8)
	v_mfma_f32_32x32x16_bf16 v[114:129], v[230:233], v[142:145], v[114:129]
	s_waitcnt lgkmcnt(7)
	v_mfma_f32_32x32x16_bf16 v[70:85], v[66:69], v[170:173], v[70:85]
	s_waitcnt lgkmcnt(6)
	v_mfma_f32_32x32x16_bf16 v[70:85], v[234:237], v[166:169], v[70:85]
	s_waitcnt lgkmcnt(5)
	v_mfma_f32_32x32x16_bf16 v[70:85], v[86:89], v[162:165], v[70:85]
	s_waitcnt lgkmcnt(4)
	v_mfma_f32_32x32x16_bf16 v[70:85], v[90:93], v[158:161], v[70:85]
	s_waitcnt lgkmcnt(3)
	v_mfma_f32_32x32x16_bf16 v[70:85], v[94:97], v[154:157], v[70:85]
	s_waitcnt lgkmcnt(2)
	v_mfma_f32_32x32x16_bf16 v[70:85], v[218:221], v[150:153], v[70:85]
	s_waitcnt lgkmcnt(1)
	v_mfma_f32_32x32x16_bf16 v[70:85], v[222:225], v[146:149], v[70:85]
	s_waitcnt lgkmcnt(0)
	v_mfma_f32_32x32x16_bf16 v[70:85], v[226:229], v[142:145], v[70:85]
	v_exp_f32_e32 v110, v110
	v_exp_f32_e32 v111, v1
	v_exp_f32_e32 v134, v104
	v_exp_f32_e32 v136, v105
	v_exp_f32_e32 v112, v112
	v_exp_f32_e32 v138, v102
	v_exp_f32_e32 v113, v113
	v_exp_f32_e32 v140, v103
	v_exp_f32_e32 v108, v108
	v_exp_f32_e32 v180, v100
	v_exp_f32_e32 v109, v109
	v_exp_f32_e32 v182, v101
	v_exp_f32_e32 v184, v98
	v_exp_f32_e32 v219, v99
	v_add_f32_e32 v1, v133, v141
	v_add_f32_e32 v98, v131, v139
	v_add_f32_e32 v99, v110, v111
	v_add_f32_e32 v100, v134, v136
	v_add_u32_e32 v178, s4, v206
	ds_read_b64_tr_b16 v[66:67], v178 offset:0
	v_exp_f32_e32 v130, v106
	v_add_f32_e32 v1, v137, v1
	v_add_f32_e32 v98, v135, v98
	v_add_f32_e32 v99, v112, v99
	v_add_f32_e32 v100, v138, v100
	ds_read_b64_tr_b16 v[68:69], v178 offset:0x800
	v_exp_f32_e32 v132, v107
	v_add_f32_e32 v1, v183, v1
	v_add_f32_e32 v98, v181, v98
	v_add_f32_e32 v99, v113, v99
	v_add_f32_e32 v100, v140, v100
	ds_read_b64_tr_b16 v[86:87], v178 offset:0x1000
	v_add_f32_e32 v1, v179, v1
	v_add_f32_e32 v98, v177, v98
	v_add_f32_e32 v99, v108, v99
	v_add_f32_e32 v100, v180, v100
	ds_read_b64_tr_b16 v[88:89], v178 offset:0x1800
	v_add_f32_e32 v1, v191, v1
	v_add_f32_e32 v98, v189, v98
	v_add_f32_e32 v99, v109, v99
	v_add_f32_e32 v100, v182, v100
	ds_read_b64_tr_b16 v[90:91], v178 offset:0x2000
	v_add_f32_e32 v1, v187, v1
	v_add_f32_e32 v98, v185, v98
	v_add_f32_e32 v99, v130, v99
	v_add_f32_e32 v100, v184, v100
	ds_read_b64_tr_b16 v[92:93], v178 offset:0x2800
	v_add_f32_e32 v1, v195, v1
	v_add_f32_e32 v98, v193, v98
	v_add_f32_e32 v99, v132, v99
	v_add_f32_e32 v100, v219, v100
	ds_read_b64_tr_b16 v[94:95], v178 offset:0x3000
	v_add_f32_e32 v1, v98, v1
	v_add_f32_e32 v98, v100, v99
	ds_read_b64_tr_b16 v[96:97], v178 offset:0x3800
	v_add_f32_e32 v1, v1, v98
	v_mov_b32_e32 v218, v1
	s_nop 1
	v_permlane32_swap_b32_e32 v1, v218
	v_cvt_pk_bf16_f32 v98, v133, v141
	v_cvt_pk_bf16_f32 v99, v137, v183
	v_cvt_pk_bf16_f32 v100, v179, v191
	v_cvt_pk_bf16_f32 v101, v187, v195
	v_cvt_pk_bf16_f32 v102, v131, v139
	v_cvt_pk_bf16_f32 v103, v135, v181
	v_cvt_pk_bf16_f32 v104, v177, v189
	v_cvt_pk_bf16_f32 v105, v185, v193
	v_cvt_pk_bf16_f32 v106, v110, v111
	v_cvt_pk_bf16_f32 v107, v112, v113
	v_cvt_pk_bf16_f32 v108, v108, v109
	v_cvt_pk_bf16_f32 v109, v130, v132
	v_cvt_pk_bf16_f32 v110, v134, v136
	v_cvt_pk_bf16_f32 v111, v138, v140
	v_cvt_pk_bf16_f32 v112, v180, v182
	v_cvt_pk_bf16_f32 v113, v184, v219
	ds_read_b64_tr_b16 v[130:131], v178 offset:0x200
	ds_read_b64_tr_b16 v[132:133], v178 offset:0xa00
	ds_read_b64_tr_b16 v[134:135], v178 offset:0x1200
	ds_read_b64_tr_b16 v[136:137], v178 offset:0x1a00
	ds_read_b64_tr_b16 v[138:139], v178 offset:0x2200
	ds_read_b64_tr_b16 v[140:141], v178 offset:0x2a00
	ds_read_b64_tr_b16 v[220:221], v178 offset:0x3200
	ds_read_b64_tr_b16 v[222:223], v178 offset:0x3a00
	s_waitcnt lgkmcnt(8)
	v_mfma_f32_32x32x16_bf16 v[50:65], v[98:101], v[66:69], v[50:65]
	v_mfma_f32_32x32x16_bf16 v[50:65], v[102:105], v[86:89], v[50:65]
	v_mfma_f32_32x32x16_bf16 v[50:65], v[106:109], v[90:93], v[50:65]
	v_mfma_f32_32x32x16_bf16 v[50:65], v[110:113], v[94:97], v[50:65]
	ds_read_b64_tr_b16 v[66:67], v178 offset:0x400
	ds_read_b64_tr_b16 v[68:69], v178 offset:0xc00
	ds_read_b64_tr_b16 v[86:87], v178 offset:0x1400
	ds_read_b64_tr_b16 v[88:89], v178 offset:0x1c00
	ds_read_b64_tr_b16 v[90:91], v178 offset:0x2400
	ds_read_b64_tr_b16 v[92:93], v178 offset:0x2c00
	ds_read_b64_tr_b16 v[94:95], v178 offset:0x3400
	ds_read_b64_tr_b16 v[96:97], v178 offset:0x3c00
	s_waitcnt lgkmcnt(8)
	v_mfma_f32_32x32x16_bf16 v[34:49], v[98:101], v[130:133], v[34:49]
	v_mfma_f32_32x32x16_bf16 v[34:49], v[102:105], v[134:137], v[34:49]
	v_mfma_f32_32x32x16_bf16 v[34:49], v[106:109], v[138:141], v[34:49]
	v_mfma_f32_32x32x16_bf16 v[34:49], v[110:113], v[220:223], v[34:49]
	ds_read_b64_tr_b16 v[130:131], v178 offset:0x600
	ds_read_b64_tr_b16 v[132:133], v178 offset:0xe00
	ds_read_b64_tr_b16 v[134:135], v178 offset:0x1600
	ds_read_b64_tr_b16 v[136:137], v178 offset:0x1e00
	ds_read_b64_tr_b16 v[138:139], v178 offset:0x2600
	ds_read_b64_tr_b16 v[140:141], v178 offset:0x2e00
	ds_read_b64_tr_b16 v[220:221], v178 offset:0x3600
	ds_read_b64_tr_b16 v[222:223], v178 offset:0x3e00
	s_waitcnt lgkmcnt(8)
	v_mfma_f32_32x32x16_bf16 v[18:33], v[98:101], v[66:69], v[18:33]
	v_mfma_f32_32x32x16_bf16 v[18:33], v[102:105], v[86:89], v[18:33]
	v_mfma_f32_32x32x16_bf16 v[18:33], v[106:109], v[90:93], v[18:33]
	v_mfma_f32_32x32x16_bf16 v[18:33], v[110:113], v[94:97], v[18:33]
	s_waitcnt lgkmcnt(0)
	v_mfma_f32_32x32x16_bf16 v[2:17], v[98:101], v[130:133], v[2:17]
	s_add_i32 s4, s89, 64
	s_cmp_le_i32 s4, s66
	v_mfma_f32_32x32x16_bf16 v[2:17], v[102:105], v[134:137], v[2:17]
	v_mfma_f32_32x32x16_bf16 v[2:17], v[106:109], v[138:141], v[2:17]
	v_mfma_f32_32x32x16_bf16 v[2:17], v[110:113], v[220:223], v[2:17]
	s_cbranch_scc1 .LBB0_262
	v_subrev_u32_e32 v66, 64, v212
	v_cmp_gt_i32_e64 s[62:63], 26, v66
	v_cmp_gt_i32_e64 s[64:65], 27, v66
	v_cmp_gt_i32_e64 s[60:61], 25, v66
	s_and_b64 s[62:63], s[64:65], s[62:63]
	v_cmp_gt_i32_e64 s[58:59], 24, v66
	s_and_b64 s[60:61], s[62:63], s[60:61]
	v_cmp_gt_i32_e64 s[56:57], 19, v66
	s_and_b64 s[58:59], s[60:61], s[58:59]
	v_cmp_gt_i32_e64 s[54:55], 18, v66
	s_and_b64 s[56:57], s[58:59], s[56:57]
	v_cmp_gt_i32_e64 s[52:53], 17, v66
	s_and_b64 s[54:55], s[56:57], s[54:55]
	v_cmp_gt_i32_e64 s[50:51], 16, v66
	s_and_b64 s[52:53], s[54:55], s[52:53]
	v_cmp_gt_i32_e64 s[48:49], 11, v66
	s_and_b64 s[50:51], s[52:53], s[50:51]
	v_cmp_gt_i32_e64 s[46:47], 10, v66
	s_and_b64 s[48:49], s[50:51], s[48:49]
	v_cmp_gt_i32_e64 s[44:45], 9, v66
	s_and_b64 s[46:47], s[48:49], s[46:47]
	v_cmp_gt_i32_e64 s[42:43], 8, v66
	s_and_b64 s[44:45], s[46:47], s[44:45]
	v_cmp_gt_i32_e64 s[40:41], 3, v66
	s_and_b64 s[42:43], s[44:45], s[42:43]
	v_cmp_gt_i32_e64 s[38:39], 2, v66
	s_and_b64 s[40:41], s[42:43], s[40:41]
	v_cmp_gt_i32_e64 s[36:37], 1, v66
	s_and_b64 s[38:39], s[40:41], s[38:39]
	v_cmp_gt_i32_e64 s[34:35], 0, v66
	s_and_b64 s[36:37], s[38:39], s[36:37]
	s_and_b64 s[34:35], s[36:37], s[34:35]
	v_cmp_gt_i32_e64 s[30:31], 58, v66
	v_cndmask_b32_e64 v114, v114, v199, s[34:35]
	v_cmp_gt_i32_e64 s[34:35], 59, v66
	v_cmp_gt_i32_e64 s[28:29], 57, v66
	s_and_b64 s[30:31], s[34:35], s[30:31]
	v_cmp_gt_i32_e64 s[26:27], 56, v66
	s_and_b64 s[28:29], s[30:31], s[28:29]
	v_cmp_gt_i32_e64 s[24:25], 51, v66
	s_and_b64 s[26:27], s[28:29], s[26:27]
	v_cmp_gt_i32_e64 s[22:23], 50, v66
	s_and_b64 s[24:25], s[26:27], s[24:25]
	v_cmp_gt_i32_e64 s[20:21], 49, v66
	s_and_b64 s[22:23], s[24:25], s[22:23]
	v_cmp_gt_i32_e64 s[18:19], 48, v66
	s_and_b64 s[20:21], s[22:23], s[20:21]
	v_cmp_gt_i32_e64 s[16:17], 43, v66
	s_and_b64 s[18:19], s[20:21], s[18:19]
	v_cmp_gt_i32_e64 s[14:15], 42, v66
	s_and_b64 s[16:17], s[18:19], s[16:17]
	v_cmp_gt_i32_e64 s[12:13], 41, v66
	s_and_b64 s[14:15], s[16:17], s[14:15]
	v_cmp_gt_i32_e64 s[10:11], 40, v66
	s_and_b64 s[12:13], s[14:15], s[12:13]
	v_cmp_gt_i32_e64 s[8:9], 35, v66
	s_and_b64 s[10:11], s[12:13], s[10:11]
	v_cmp_gt_i32_e64 s[6:7], 34, v66
	s_and_b64 s[8:9], s[10:11], s[8:9]
	v_cmp_gt_i32_e64 s[4:5], 33, v66
	s_and_b64 s[6:7], s[8:9], s[6:7]
	v_cmp_gt_i32_e32 vcc, 32, v66
	s_and_b64 s[4:5], s[6:7], s[4:5]
	s_and_b64 vcc, s[4:5], vcc
	v_cndmask_b32_e64 v129, v129, v199, s[64:65]
	v_cndmask_b32_e64 v128, v128, v199, s[62:63]
	v_cndmask_b32_e64 v127, v127, v199, s[60:61]
	v_cndmask_b32_e64 v126, v126, v199, s[58:59]
	v_cndmask_b32_e64 v125, v125, v199, s[56:57]
	v_cndmask_b32_e64 v124, v124, v199, s[54:55]
	v_cndmask_b32_e64 v123, v123, v199, s[52:53]
	v_cndmask_b32_e64 v122, v122, v199, s[50:51]
	v_cndmask_b32_e64 v121, v121, v199, s[48:49]
	v_cndmask_b32_e64 v120, v120, v199, s[46:47]
	v_cndmask_b32_e64 v119, v119, v199, s[44:45]
	v_cndmask_b32_e64 v118, v118, v199, s[42:43]
	v_cndmask_b32_e64 v117, v117, v199, s[40:41]
	v_cndmask_b32_e64 v116, v116, v199, s[38:39]
	v_cndmask_b32_e64 v115, v115, v199, s[36:37]
	v_cndmask_b32_e64 v85, v85, v199, s[34:35]
	v_cndmask_b32_e64 v84, v84, v199, s[30:31]
	v_cndmask_b32_e64 v83, v83, v199, s[28:29]
	v_cndmask_b32_e64 v82, v82, v199, s[26:27]
	v_cndmask_b32_e64 v81, v81, v199, s[24:25]
	v_cndmask_b32_e64 v80, v80, v199, s[22:23]
	v_cndmask_b32_e64 v79, v79, v199, s[20:21]
	v_cndmask_b32_e64 v78, v78, v199, s[18:19]
	v_cndmask_b32_e64 v77, v77, v199, s[16:17]
	v_cndmask_b32_e64 v76, v76, v199, s[14:15]
	v_cndmask_b32_e64 v75, v75, v199, s[12:13]
	v_cndmask_b32_e64 v74, v74, v199, s[10:11]
	v_cndmask_b32_e64 v73, v73, v199, s[8:9]
	v_cndmask_b32_e64 v72, v72, v199, s[6:7]
	v_cndmask_b32_e64 v71, v71, v199, s[4:5]
	v_cndmask_b32_e32 v70, v70, v199, vcc

.LBB0_268:
	v_cndmask_b32_e64 v98, v66, v207, s[4:5]
	v_sub_f32_e32 v66, v114, v98
	v_sub_f32_e32 v67, v115, v98
	v_sub_f32_e32 v68, v116, v98
	v_sub_f32_e32 v69, v117, v98
	v_sub_f32_e32 v86, v118, v98
	v_sub_f32_e32 v87, v119, v98
	v_sub_f32_e32 v88, v120, v98
	v_sub_f32_e32 v89, v121, v98
	v_sub_f32_e32 v90, v122, v98
	v_sub_f32_e32 v91, v123, v98
	v_sub_f32_e32 v92, v124, v98
	v_sub_f32_e32 v93, v125, v98
	v_sub_f32_e32 v94, v126, v98
	v_sub_f32_e32 v95, v127, v98
	v_sub_f32_e32 v96, v128, v98
	v_sub_f32_e32 v97, v129, v98
	v_sub_f32_e32 v99, v70, v98
	v_sub_f32_e32 v108, v71, v98
	v_sub_f32_e32 v109, v72, v98
	v_sub_f32_e32 v177, v73, v98
	v_sub_f32_e32 v178, v74, v98
	v_sub_f32_e32 v179, v75, v98
	v_sub_f32_e32 v180, v76, v98
	v_sub_f32_e32 v181, v77, v98
	v_sub_f32_e32 v182, v78, v98
	v_sub_f32_e32 v183, v79, v98
	v_sub_f32_e32 v184, v80, v98
	v_sub_f32_e32 v185, v81, v98
	v_exp_f32_e32 v66, v66
	v_exp_f32_e32 v67, v67
	v_exp_f32_e32 v68, v68
	v_exp_f32_e32 v69, v69
	v_exp_f32_e32 v70, v86
	v_exp_f32_e32 v71, v87
	v_exp_f32_e32 v72, v88
	v_exp_f32_e32 v73, v89
	v_exp_f32_e32 v74, v90
	v_exp_f32_e32 v75, v91
	v_exp_f32_e32 v76, v92
	v_exp_f32_e32 v77, v93
	v_exp_f32_e32 v78, v94
	v_exp_f32_e32 v79, v95
	v_exp_f32_e32 v80, v96
	v_exp_f32_e32 v81, v97
	v_sub_f32_e32 v187, v82, v98
	v_sub_f32_e32 v189, v83, v98
	v_sub_f32_e32 v191, v84, v98
	v_sub_f32_e32 v193, v85, v98
	ds_read_b128 v[126:129], v213
	ds_read_b128 v[130:133], v213 offset:32
	ds_read_b128 v[110:113], v213 offset:128
	ds_read_b128 v[114:117], v213 offset:160
	ds_read_b128 v[134:137], v213 offset:64
	ds_read_b128 v[138:141], v213 offset:96
	ds_read_b128 v[118:121], v213 offset:192
	ds_read_b128 v[122:125], v213 offset:224
	ds_read_b128 v[82:85], v188 offset:49152
	ds_read_b128 v[86:89], v190 offset:49152
	ds_read_b128 v[90:93], v192 offset:49152
	ds_read_b128 v[94:97], v194 offset:49152
	ds_read_b128 v[100:103], v188 offset:49280
	ds_read_b128 v[104:107], v190 offset:49280
	ds_read_b128 v[220:223], v192 offset:49280
	ds_read_b128 v[224:227], v194 offset:49280
	s_waitcnt lgkmcnt(7)
	v_mfma_f32_32x32x16_bf16 v[126:141], v[82:85], v[170:173], v[126:141]
	ds_read_b128 v[82:85], v188 offset:57344
	ds_read_b128 v[228:231], v190 offset:57344
	s_waitcnt lgkmcnt(8)
	v_mfma_f32_32x32x16_bf16 v[126:141], v[86:89], v[166:169], v[126:141]
	ds_read_b128 v[86:89], v192 offset:57344
	s_waitcnt lgkmcnt(8)
	v_mfma_f32_32x32x16_bf16 v[126:141], v[90:93], v[162:165], v[126:141]
	ds_read_b128 v[90:93], v194 offset:57344
	s_waitcnt lgkmcnt(8)
	v_mfma_f32_32x32x16_bf16 v[126:141], v[94:97], v[158:161], v[126:141]
	ds_read_b128 v[94:97], v188 offset:57472
	s_waitcnt lgkmcnt(8)
	v_mfma_f32_32x32x16_bf16 v[126:141], v[100:103], v[154:157], v[126:141]
	ds_read_b128 v[100:103], v190 offset:57472
	s_waitcnt lgkmcnt(8)
	v_mfma_f32_32x32x16_bf16 v[126:141], v[104:107], v[150:153], v[126:141]
	ds_read_b128 v[104:107], v192 offset:57472
	s_waitcnt lgkmcnt(8)
	v_mfma_f32_32x32x16_bf16 v[126:141], v[220:223], v[146:149], v[126:141]
	ds_read_b128 v[220:223], v194 offset:57472
	s_waitcnt lgkmcnt(8)
	v_mfma_f32_32x32x16_bf16 v[126:141], v[224:227], v[142:145], v[126:141]
	s_waitcnt lgkmcnt(7)
	v_mfma_f32_32x32x16_bf16 v[110:125], v[82:85], v[170:173], v[110:125]
	s_waitcnt lgkmcnt(6)
	v_mfma_f32_32x32x16_bf16 v[110:125], v[228:231], v[166:169], v[110:125]
	s_waitcnt lgkmcnt(5)
	v_mfma_f32_32x32x16_bf16 v[110:125], v[86:89], v[162:165], v[110:125]
	s_waitcnt lgkmcnt(4)
	v_mfma_f32_32x32x16_bf16 v[110:125], v[90:93], v[158:161], v[110:125]
	s_waitcnt lgkmcnt(3)
	v_mfma_f32_32x32x16_bf16 v[110:125], v[94:97], v[154:157], v[110:125]
	s_waitcnt lgkmcnt(2)
	v_mfma_f32_32x32x16_bf16 v[110:125], v[100:103], v[150:153], v[110:125]
	s_waitcnt lgkmcnt(1)
	v_mfma_f32_32x32x16_bf16 v[110:125], v[104:107], v[146:149], v[110:125]
	s_waitcnt lgkmcnt(0)
	v_mfma_f32_32x32x16_bf16 v[110:125], v[220:223], v[142:145], v[110:125]
	v_exp_f32_e32 v82, v99
	v_exp_f32_e32 v83, v108
	v_exp_f32_e32 v90, v182
	v_exp_f32_e32 v91, v183
	v_exp_f32_e32 v84, v109
	v_exp_f32_e32 v92, v184
	v_exp_f32_e32 v85, v177
	v_exp_f32_e32 v93, v185
	v_exp_f32_e32 v86, v178
	v_exp_f32_e32 v94, v187
	v_exp_f32_e32 v87, v179
	v_exp_f32_e32 v95, v189
	v_add_f32_e32 v99, v66, v67
	v_add_f32_e32 v108, v74, v75
	v_add_f32_e32 v109, v82, v83
	v_add_f32_e32 v177, v90, v91
	v_add_u32_e32 v195, s33, v206
	ds_read_b64_tr_b16 v[100:101], v195 offset:0
	v_exp_f32_e32 v88, v180
	v_exp_f32_e32 v96, v191
	v_add_f32_e32 v99, v68, v99
	v_add_f32_e32 v108, v76, v108
	v_add_f32_e32 v109, v84, v109
	v_add_f32_e32 v177, v92, v177
	ds_read_b64_tr_b16 v[102:103], v195 offset:0x800
	v_exp_f32_e32 v89, v181
	v_exp_f32_e32 v97, v193
	v_add_f32_e32 v99, v69, v99
	v_add_f32_e32 v108, v77, v108
	v_add_f32_e32 v109, v85, v109
	v_add_f32_e32 v177, v93, v177
	ds_read_b64_tr_b16 v[104:105], v195 offset:0x1000
	v_add_f32_e32 v99, v70, v99
	v_add_f32_e32 v108, v78, v108
	v_add_f32_e32 v109, v86, v109
	v_add_f32_e32 v177, v94, v177
	ds_read_b64_tr_b16 v[106:107], v195 offset:0x1800
	v_add_f32_e32 v99, v71, v99
	v_add_f32_e32 v108, v79, v108
	v_add_f32_e32 v109, v87, v109
	v_add_f32_e32 v177, v95, v177
	ds_read_b64_tr_b16 v[222:223], v195 offset:0x2000
	v_add_f32_e32 v99, v72, v99
	v_add_f32_e32 v108, v80, v108
	v_add_f32_e32 v109, v88, v109
	v_add_f32_e32 v177, v96, v177
	ds_read_b64_tr_b16 v[224:225], v195 offset:0x2800
	v_add_f32_e32 v99, v73, v99
	v_add_f32_e32 v108, v81, v108
	v_add_f32_e32 v109, v89, v109
	v_add_f32_e32 v177, v97, v177
	ds_read_b64_tr_b16 v[226:227], v195 offset:0x3000
	v_add_f32_e32 v99, v108, v99
	v_add_f32_e32 v108, v177, v109
	ds_read_b64_tr_b16 v[228:229], v195 offset:0x3800
	v_add_f32_e32 v220, v108, v99
	v_mov_b32_e32 v221, v220
	s_nop 1
	v_permlane32_swap_b32_e32 v220, v221
	v_cvt_pk_bf16_f32 v230, v66, v67
	v_cvt_pk_bf16_f32 v231, v68, v69
	v_cvt_pk_bf16_f32 v232, v70, v71
	v_cvt_pk_bf16_f32 v233, v72, v73
	v_cvt_pk_bf16_f32 v234, v74, v75
	v_cvt_pk_bf16_f32 v235, v76, v77
	v_cvt_pk_bf16_f32 v236, v78, v79
	v_cvt_pk_bf16_f32 v237, v80, v81
	v_cvt_pk_bf16_f32 v238, v82, v83
	v_cvt_pk_bf16_f32 v239, v84, v85
	v_cvt_pk_bf16_f32 v240, v86, v87
	v_cvt_pk_bf16_f32 v241, v88, v89
	v_cvt_pk_bf16_f32 v242, v90, v91
	v_cvt_pk_bf16_f32 v243, v92, v93
	v_cvt_pk_bf16_f32 v244, v94, v95
	v_cvt_pk_bf16_f32 v245, v96, v97
	ds_read_b64_tr_b16 v[246:247], v195 offset:0x200
	ds_read_b64_tr_b16 v[248:249], v195 offset:0xa00
	ds_read_b64_tr_b16 v[250:251], v195 offset:0x1200
	ds_read_b64_tr_b16 v[252:253], v195 offset:0x1a00
	ds_read_b64_tr_b16 v[178:179], v195 offset:0x2200
	ds_read_b64_tr_b16 v[180:181], v195 offset:0x2a00
	ds_read_b64_tr_b16 v[182:183], v195 offset:0x3200
	ds_read_b64_tr_b16 v[184:185], v195 offset:0x3a00
	s_waitcnt lgkmcnt(8)
	v_mfma_f32_32x32x16_bf16 v[50:65], v[230:233], v[100:103], v[50:65]
	v_mfma_f32_32x32x16_bf16 v[50:65], v[234:237], v[104:107], v[50:65]
	v_mfma_f32_32x32x16_bf16 v[50:65], v[238:241], v[222:225], v[50:65]
	v_mfma_f32_32x32x16_bf16 v[50:65], v[242:245], v[226:229], v[50:65]
	ds_read_b64_tr_b16 v[100:101], v195 offset:0x400
	ds_read_b64_tr_b16 v[102:103], v195 offset:0xc00
	ds_read_b64_tr_b16 v[104:105], v195 offset:0x1400
	ds_read_b64_tr_b16 v[106:107], v195 offset:0x1c00
	ds_read_b64_tr_b16 v[222:223], v195 offset:0x2400
	ds_read_b64_tr_b16 v[224:225], v195 offset:0x2c00
	ds_read_b64_tr_b16 v[226:227], v195 offset:0x3400
	ds_read_b64_tr_b16 v[228:229], v195 offset:0x3c00
	s_waitcnt lgkmcnt(8)
	v_mfma_f32_32x32x16_bf16 v[34:49], v[230:233], v[246:249], v[34:49]
	v_mfma_f32_32x32x16_bf16 v[34:49], v[234:237], v[250:253], v[34:49]
	v_mfma_f32_32x32x16_bf16 v[34:49], v[238:241], v[178:181], v[34:49]
	v_mfma_f32_32x32x16_bf16 v[34:49], v[242:245], v[182:185], v[34:49]
	ds_read_b64_tr_b16 v[178:179], v195 offset:0x600
	ds_read_b64_tr_b16 v[180:181], v195 offset:0xe00
	ds_read_b64_tr_b16 v[182:183], v195 offset:0x1600
	ds_read_b64_tr_b16 v[184:185], v195 offset:0x1e00
	ds_read_b64_tr_b16 v[246:247], v195 offset:0x2600
	ds_read_b64_tr_b16 v[248:249], v195 offset:0x2e00
	ds_read_b64_tr_b16 v[250:251], v195 offset:0x3600
	ds_read_b64_tr_b16 v[252:253], v195 offset:0x3e00
	s_waitcnt lgkmcnt(8)
	v_mfma_f32_32x32x16_bf16 v[18:33], v[230:233], v[100:103], v[18:33]
	v_mfma_f32_32x32x16_bf16 v[18:33], v[234:237], v[104:107], v[18:33]
	v_mfma_f32_32x32x16_bf16 v[18:33], v[238:241], v[222:225], v[18:33]
	v_mfma_f32_32x32x16_bf16 v[18:33], v[242:245], v[226:229], v[18:33]
	s_waitcnt lgkmcnt(0)
	v_mfma_f32_32x32x16_bf16 v[2:17], v[230:233], v[178:181], v[2:17]
	s_cmp_le_i32 s89, s66
	v_mfma_f32_32x32x16_bf16 v[2:17], v[234:237], v[182:185], v[2:17]
	v_mfma_f32_32x32x16_bf16 v[2:17], v[238:241], v[246:249], v[2:17]
	v_mfma_f32_32x32x16_bf16 v[2:17], v[242:245], v[250:253], v[2:17]
	s_cbranch_scc1 .LBB0_270
	v_cmp_gt_i32_e64 s[62:63], 26, v212
	v_cmp_gt_i32_e64 s[64:65], 27, v212
	v_cmp_gt_i32_e64 s[60:61], 25, v212
	s_and_b64 s[62:63], s[64:65], s[62:63]
	v_cmp_gt_i32_e64 s[58:59], 24, v212
	s_and_b64 s[60:61], s[62:63], s[60:61]
	v_cmp_gt_i32_e64 s[56:57], 19, v212
	s_and_b64 s[58:59], s[60:61], s[58:59]
	v_cmp_gt_i32_e64 s[54:55], 18, v212
	s_and_b64 s[56:57], s[58:59], s[56:57]
	v_cmp_gt_i32_e64 s[52:53], 17, v212
	s_and_b64 s[54:55], s[56:57], s[54:55]
	v_cmp_gt_i32_e64 s[50:51], 16, v212
	s_and_b64 s[52:53], s[54:55], s[52:53]
	v_cmp_gt_i32_e64 s[48:49], 11, v212
	s_and_b64 s[50:51], s[52:53], s[50:51]
	v_cmp_gt_i32_e64 s[46:47], 10, v212
	s_and_b64 s[48:49], s[50:51], s[48:49]
	v_cmp_gt_i32_e64 s[44:45], 9, v212
	s_and_b64 s[46:47], s[48:49], s[46:47]
	v_cmp_gt_i32_e64 s[42:43], 8, v212
	s_and_b64 s[44:45], s[46:47], s[44:45]
	v_cmp_gt_i32_e64 s[40:41], 3, v212
	s_and_b64 s[42:43], s[44:45], s[42:43]
	v_cmp_gt_i32_e64 s[38:39], 2, v212
	s_and_b64 s[40:41], s[42:43], s[40:41]
	v_cmp_gt_i32_e64 s[36:37], 1, v212
	s_and_b64 s[38:39], s[40:41], s[38:39]
	v_cmp_gt_i32_e64 s[34:35], 0, v212
	s_and_b64 s[36:37], s[38:39], s[36:37]
	s_and_b64 s[34:35], s[36:37], s[34:35]
	v_cmp_gt_i32_e64 s[30:31], 58, v212
	v_cndmask_b32_e64 v126, v126, v199, s[34:35]
	v_cmp_gt_i32_e64 s[34:35], 59, v212
	v_cmp_gt_i32_e64 s[28:29], 57, v212
	s_and_b64 s[30:31], s[34:35], s[30:31]
	v_cmp_gt_i32_e64 s[26:27], 56, v212
	s_and_b64 s[28:29], s[30:31], s[28:29]
	v_cmp_gt_i32_e64 s[24:25], 51, v212
	s_and_b64 s[26:27], s[28:29], s[26:27]
	v_cmp_gt_i32_e64 s[22:23], 50, v212
	s_and_b64 s[24:25], s[26:27], s[24:25]
	v_cmp_gt_i32_e64 s[20:21], 49, v212
	s_and_b64 s[22:23], s[24:25], s[22:23]
	v_cmp_gt_i32_e64 s[18:19], 48, v212
	s_and_b64 s[20:21], s[22:23], s[20:21]
	v_cmp_gt_i32_e64 s[16:17], 43, v212
	s_and_b64 s[18:19], s[20:21], s[18:19]
	v_cmp_gt_i32_e64 s[14:15], 42, v212
	s_and_b64 s[16:17], s[18:19], s[16:17]
	v_cmp_gt_i32_e64 s[12:13], 41, v212
	s_and_b64 s[14:15], s[16:17], s[14:15]
	v_cmp_gt_i32_e64 s[10:11], 40, v212
	s_and_b64 s[12:13], s[14:15], s[12:13]
	v_cmp_gt_i32_e64 s[8:9], 35, v212
	s_and_b64 s[10:11], s[12:13], s[10:11]
	v_cmp_gt_i32_e64 s[6:7], 34, v212
	s_and_b64 s[8:9], s[10:11], s[8:9]
	v_cmp_gt_i32_e64 s[4:5], 33, v212
	s_and_b64 s[6:7], s[8:9], s[6:7]
	v_cmp_gt_i32_e32 vcc, 32, v212
	s_and_b64 s[4:5], s[6:7], s[4:5]
	s_and_b64 vcc, s[4:5], vcc
	v_cndmask_b32_e64 v141, v141, v199, s[64:65]
	v_cndmask_b32_e64 v140, v140, v199, s[62:63]
	v_cndmask_b32_e64 v139, v139, v199, s[60:61]
	v_cndmask_b32_e64 v138, v138, v199, s[58:59]
	v_cndmask_b32_e64 v137, v137, v199, s[56:57]
	v_cndmask_b32_e64 v136, v136, v199, s[54:55]
	v_cndmask_b32_e64 v135, v135, v199, s[52:53]
	v_cndmask_b32_e64 v134, v134, v199, s[50:51]
	v_cndmask_b32_e64 v133, v133, v199, s[48:49]
	v_cndmask_b32_e64 v132, v132, v199, s[46:47]
	v_cndmask_b32_e64 v131, v131, v199, s[44:45]
	v_cndmask_b32_e64 v130, v130, v199, s[42:43]
	v_cndmask_b32_e64 v129, v129, v199, s[40:41]
	v_cndmask_b32_e64 v128, v128, v199, s[38:39]
	v_cndmask_b32_e64 v127, v127, v199, s[36:37]
	v_cndmask_b32_e64 v125, v125, v199, s[34:35]
	v_cndmask_b32_e64 v124, v124, v199, s[30:31]
	v_cndmask_b32_e64 v123, v123, v199, s[28:29]
	v_cndmask_b32_e64 v122, v122, v199, s[26:27]
	v_cndmask_b32_e64 v121, v121, v199, s[24:25]
	v_cndmask_b32_e64 v120, v120, v199, s[22:23]
	v_cndmask_b32_e64 v119, v119, v199, s[20:21]
	v_cndmask_b32_e64 v118, v118, v199, s[18:19]
	v_cndmask_b32_e64 v117, v117, v199, s[16:17]
	v_cndmask_b32_e64 v116, v116, v199, s[14:15]
	v_cndmask_b32_e64 v115, v115, v199, s[12:13]
	v_cndmask_b32_e64 v114, v114, v199, s[10:11]
	v_cndmask_b32_e64 v113, v113, v199, s[8:9]
	v_cndmask_b32_e64 v112, v112, v199, s[6:7]
	v_cndmask_b32_e64 v111, v111, v199, s[4:5]
	v_cndmask_b32_e32 v110, v110, v199, vcc
